# P2 inner loop VALU trimming: persistent ones operand in v[240:243] for the row-sum MFMAs, v_max3 row-max tree without self-max canonicalisation, V-fragment reads take their address registers directly
# baseline (speedup 1.0000x reference)
.LBB0_255:
	v_writelane_b32 v238, s22, 17
	s_mov_b32 s1, 0
	v_and_b32_e32 v182, 48, v5
	v_writelane_b32 v238, s23, 18
	v_writelane_b32 v238, s0, 19
	v_bfe_u32 v5, v4, 5, 1
	v_and_b32_e32 v187, 31, v4
	v_writelane_b32 v238, s1, 20
	v_cmp_eq_u32_e64 s[0:1], 0, v6
	v_lshlrev_b32_e32 v6, 2, v5
	v_sub_u32_e32 v6, v187, v6
	v_mov_b32_e32 v195, 0xff800000
	v_cmp_gt_i32_e32 vcc, 0, v6
	v_and_b32_e32 v7, 7, v4
	v_writelane_b32 v238, s0, 21
	v_cndmask_b32_e32 v18, 0, v195, vcc
	v_cmp_gt_i32_e32 vcc, 1, v6
	v_and_b32_e32 v3, 63, v4
	v_lshlrev_b32_e32 v2, 5, v7
	v_cndmask_b32_e32 v19, 0, v195, vcc
	v_cmp_gt_i32_e32 vcc, 2, v6
	v_writelane_b32 v238, s1, 22
	v_add_u32_e32 v194, 0x80, v6
	v_cndmask_b32_e32 v20, 0, v195, vcc
	v_cmp_gt_i32_e32 vcc, 3, v6
	v_lshlrev_b32_e32 v38, 1, v4
	s_sub_i32 s0, 7, s54
	v_cndmask_b32_e32 v21, 0, v195, vcc
	v_cmp_gt_i32_e32 vcc, 8, v6
	v_and_b32_e32 v184, 32, v4
	v_add_u32_e32 v8, 0xffffff80, v2
	v_cndmask_b32_e32 v22, 0, v195, vcc
	v_cmp_gt_i32_e32 vcc, 9, v6
	v_lshlrev_b32_e32 v9, 5, v1
	s_movk_i32 s38, 0x90
	v_cndmask_b32_e32 v23, 0, v195, vcc
	v_cmp_gt_i32_e32 vcc, 10, v6
	s_cmp_gt_i32 s54, 3
	v_bitop3_b32 v8, v8, v9, 64 bitop3:0x78
	v_cndmask_b32_e32 v24, 0, v195, vcc
	v_cmp_gt_i32_e32 vcc, 11, v6
	v_lshlrev_b32_e32 v9, 7, v1
	v_mul_lo_u32 v10, v1, s38
	v_cndmask_b32_e32 v25, 0, v195, vcc
	v_cmp_gt_i32_e32 vcc, 16, v6
	s_cselect_b32 s89, s0, s54
	v_cmp_gt_u32_e64 s[0:1], 32, v3
	v_cndmask_b32_e32 v26, 0, v195, vcc
	v_cmp_gt_i32_e32 vcc, 17, v6
	v_add3_u32 v8, 0, v8, v9
	v_add3_u32 v10, 0, v2, v10
	v_cndmask_b32_e32 v27, 0, v195, vcc
	v_cmp_gt_i32_e32 vcc, 18, v6
	v_and_b32_e32 v38, 32, v38
	v_add_u32_e32 v9, 0xd800, v8
	v_cndmask_b32_e32 v28, 0, v195, vcc
	v_cmp_gt_i32_e32 vcc, 19, v6
	v_add_u32_e32 v11, 0xf800, v8
	v_add_u32_e32 v12, 0x2400, v10
	v_cndmask_b32_e32 v29, 0, v195, vcc
	v_cmp_gt_i32_e32 vcc, 24, v6
	v_add_u32_e32 v13, 0x11800, v8
	v_add_u32_e32 v14, 0x4800, v10
	v_cndmask_b32_e32 v30, 0, v195, vcc
	v_cmp_gt_i32_e32 vcc, 25, v6
	v_add_u32_e32 v15, 0x13800, v8
	v_add_u32_e32 v16, 0x6c00, v10
	v_cndmask_b32_e32 v31, 0, v195, vcc
	v_cmp_gt_i32_e32 vcc, 26, v6
	v_add_u32_e32 v17, 0x15800, v8
	v_add_u32_e32 v34, 0x9000, v10
	v_cndmask_b32_e32 v32, 0, v195, vcc
	v_cmp_gt_i32_e32 vcc, 27, v6
	v_lshlrev_b32_e32 v6, 3, v4
	v_lshlrev_b32_e32 v4, 5, v4
	v_and_b32_e32 v4, 0x180, v4
	v_bitop3_b32 v3, v6, 64, v6 bitop3:0xc
	v_lshl_or_b32 v4, v5, 9, v4
	v_and_b32_e32 v36, 64, v6
	v_and_b32_e32 v37, 24, v6
	v_or_b32_e32 v3, v4, v3
	v_add_u32_e32 v8, 0x17800, v8
	v_add_u32_e32 v35, 0xb400, v10
	v_mov_b32_e32 v2, 0
	v_cndmask_b32_e32 v33, 0, v195, vcc
	v_cmp_gt_u32_e32 vcc, 4, v7
	v_or3_b32 v202, v3, v38, v37
	v_or_b32_e32 v3, v4, v36
	v_add_u32_e32 v1, 0xffffff80, v1
	v_mov_b32_e32 v183, v2
	s_ashr_i32 s52, s2, 8
	v_mov_b32_e32 v185, v2
	v_lshlrev_b32_e32 v186, 6, v5
	v_lshlrev_b32_e32 v188, 4, v5
	v_mov_b32_e32 v189, v2
	v_writelane_b32 v238, s0, 23
	v_cndmask_b32_e32 v196, v9, v10, vcc
	v_cndmask_b32_e32 v197, v11, v12, vcc
	v_cndmask_b32_e32 v198, v13, v14, vcc
	v_cndmask_b32_e32 v199, v15, v16, vcc
	v_cndmask_b32_e32 v200, v17, v34, vcc
	v_cndmask_b32_e32 v201, v8, v35, vcc
	s_ashr_i32 s75, s54, 31
	s_abs_i32 s81, s54
	v_or3_b32 v203, v3, v38, v37
	s_mov_b32 s28, 0x3f803f80
	v_mov_b32_e32 v240, s28
	v_mov_b32_e32 v241, s28
	v_mov_b32_e32 v242, s28
	v_mov_b32_e32 v243, s28
	s_mov_b32 s34, 0x3e38aa3b
	s_mov_b32 s60, s96
	v_writelane_b32 v238, s1, 24
	s_branch .LBB0_258

.LBB0_325:
	ds_read_b64_tr_b16 v[162:163], v206 offset:55296
	ds_read_b64_tr_b16 v[164:165], v206 offset:56320
	ds_read_b64_tr_b16 v[4:5], v206 offset:57344
	ds_read_b64_tr_b16 v[6:7], v206 offset:58368
	ds_read_b64_tr_b16 v[12:13], v193 offset:55296
	ds_read_b64_tr_b16 v[14:15], v193 offset:56320
	ds_read_b64_tr_b16 v[8:9], v193 offset:57344
	ds_read_b64_tr_b16 v[10:11], v193 offset:58368
	s_cmp_lg_u32 s69, s70
	s_mov_b64 s[8:9], -1
	s_cbranch_scc0 .LBB0_331
	s_cmp_lg_u32 s7, s70
	s_cbranch_scc0 .LBB0_328
	s_mov_b64 s[8:9], 0
	s_waitcnt lgkmcnt(11)
	v_mfma_f32_32x32x16_bf16 v[98:113], v[178:181], v[138:141], 0

.LBB0_333:
	s_waitcnt lgkmcnt(10)
	v_mfma_f32_32x32x16_bf16 v[98:113], v[174:177], v[142:145], v[98:113]
	s_waitcnt lgkmcnt(9)
	v_mfma_f32_32x32x16_bf16 v[98:113], v[170:173], v[146:149], v[98:113]
	s_waitcnt lgkmcnt(8)
	v_mfma_f32_32x32x16_bf16 v[98:113], v[166:169], v[150:153], v[98:113]
	s_nop 11
	ds_read_b128 v[178:181], v192 offset:4608
	ds_read_b128 v[174:177], v192 offset:4624
	ds_read_b128 v[170:173], v192 offset:4640
	ds_read_b128 v[166:169], v192 offset:4656
	v_max3_f32 v3, v98, v99, v100
	v_max3_f32 v3, v3, v101, v102
	v_max3_f32 v3, v3, v103, v104
	v_max3_f32 v3, v3, v105, v106
	v_max3_f32 v3, v3, v107, v108
	v_max3_f32 v3, v3, v109, v110
	v_max3_f32 v3, v3, v111, v112
	v_max_f32_e32 v3, v3, v113
	v_mov_b32_e32 v16, v3
	s_nop 1
	v_permlane32_swap_b32_e32 v3, v16
	v_max_f32_e32 v3, v3, v16
	v_add_f32_e32 v16, 0x41000000, v205
	v_cmp_gt_f32_e32 vcc, v3, v16
	s_cbranch_vccz .LBB0_335
	v_max_f32_e32 v3, v3, v3
	v_max_f32_e32 v16, v205, v205
	v_max_f32_e32 v3, v16, v3
	v_sub_f32_e32 v16, v205, v3
	v_exp_f32_e32 v16, v16
	v_mov_b32_e32 v205, v3
	v_mul_f32_e32 v50, v50, v16
	v_pk_mul_f32 v[80:81], v[80:81], v[16:17] op_sel_hi:[1,0]
	v_pk_mul_f32 v[78:79], v[78:79], v[16:17] op_sel_hi:[1,0]
	v_pk_mul_f32 v[76:77], v[76:77], v[16:17] op_sel_hi:[1,0]
	v_pk_mul_f32 v[74:75], v[74:75], v[16:17] op_sel_hi:[1,0]
	v_pk_mul_f32 v[72:73], v[72:73], v[16:17] op_sel_hi:[1,0]
	v_pk_mul_f32 v[70:71], v[70:71], v[16:17] op_sel_hi:[1,0]
	v_pk_mul_f32 v[68:69], v[68:69], v[16:17] op_sel_hi:[1,0]
	v_pk_mul_f32 v[66:67], v[66:67], v[16:17] op_sel_hi:[1,0]
	v_pk_mul_f32 v[96:97], v[96:97], v[16:17] op_sel_hi:[1,0]
	v_pk_mul_f32 v[94:95], v[94:95], v[16:17] op_sel_hi:[1,0]
	v_pk_mul_f32 v[92:93], v[92:93], v[16:17] op_sel_hi:[1,0]
	v_pk_mul_f32 v[90:91], v[90:91], v[16:17] op_sel_hi:[1,0]
	v_pk_mul_f32 v[88:89], v[88:89], v[16:17] op_sel_hi:[1,0]
	v_pk_mul_f32 v[86:87], v[86:87], v[16:17] op_sel_hi:[1,0]
	v_pk_mul_f32 v[84:85], v[84:85], v[16:17] op_sel_hi:[1,0]
	v_pk_mul_f32 v[82:83], v[82:83], v[16:17] op_sel_hi:[1,0]
.LBB0_335:
	v_sub_f32_e32 v3, v98, v205
	v_sub_f32_e32 v98, v101, v205
	v_sub_f32_e32 v16, v99, v205
	v_exp_f32_e32 v99, v98
	v_sub_f32_e32 v98, v102, v205
	v_sub_f32_e32 v17, v100, v205
	v_exp_f32_e32 v100, v98
	v_sub_f32_e32 v98, v103, v205
	v_exp_f32_e32 v101, v98
	v_sub_f32_e32 v98, v104, v205
	v_exp_f32_e32 v102, v98
	v_sub_f32_e32 v98, v105, v205
	v_exp_f32_e32 v103, v98
	v_sub_f32_e32 v98, v106, v205
	v_exp_f32_e32 v104, v98
	v_sub_f32_e32 v98, v107, v205
	v_exp_f32_e32 v105, v98
	v_sub_f32_e32 v98, v108, v205
	v_exp_f32_e32 v106, v98
	v_sub_f32_e32 v98, v109, v205
	v_exp_f32_e32 v3, v3
	v_exp_f32_e32 v16, v16
	v_exp_f32_e32 v17, v17
	v_exp_f32_e32 v107, v98
	v_sub_f32_e32 v98, v110, v205
	v_exp_f32_e32 v108, v98
	v_sub_f32_e32 v98, v111, v205
	v_exp_f32_e32 v109, v98
	v_sub_f32_e32 v98, v112, v205
	v_exp_f32_e32 v110, v98
	v_sub_f32_e32 v98, v113, v205
	v_exp_f32_e32 v111, v98
	v_cvt_pk_bf16_f32 v98, v3, v16
	v_cvt_pk_bf16_f32 v99, v17, v99
	v_cvt_pk_bf16_f32 v100, v100, v101
	v_cvt_pk_bf16_f32 v101, v102, v103
	s_waitcnt lgkmcnt(2)
	v_mfma_f32_32x32x16_bf16 v[82:97], v[12:15], v[98:101], v[82:97]
	v_cvt_pk_bf16_f32 v102, v104, v105
	v_cvt_pk_bf16_f32 v103, v106, v107
	v_cvt_pk_bf16_f32 v104, v108, v109
	v_cvt_pk_bf16_f32 v105, v110, v111
	v_mfma_f32_32x32x16_bf16 v[66:81], v[162:165], v[98:101], v[66:81]
	s_add_i32 s8, s70, 1
	s_add_i32 s9, s70, -4
	v_add_u32_e32 v192, 0x1200, v192
	v_add_u32_e32 v193, 0x1000, v193
	v_add_u32_e32 v206, 0x1000, v206
	s_cmp_ge_i32 s9, s7
	v_mfma_f32_32x32x16_bf16 v[50:65], v[240:243], v[98:101], v[50:65]
	v_mfma_f32_32x32x16_bf16 v[66:81], v[4:7], v[102:105], v[66:81]
	s_waitcnt lgkmcnt(0)
	v_mfma_f32_32x32x16_bf16 v[82:97], v[8:11], v[102:105], v[82:97]
	v_mfma_f32_32x32x16_bf16 v[50:65], v[240:243], v[102:105], v[50:65]
	s_cbranch_scc1 .LBB0_338
	s_mov_b32 s70, s8
	s_branch .LBB0_325
